# baseline (speedup 1.0000x reference)
.LBB2_7:
	s_mov_b32 s24, 0
	s_andn2_b64 vcc, exec, s[4:5]
	v_mov_b32_e32 v81, 0
	s_cbranch_vccnz .LBB2_28
	s_cmp_gt_i32 s23, 11
	s_cbranch_scc1 .Lmy_dp_hi
	s_cmp_gt_i32 s23, 9
	s_cbranch_scc1 .Lmy_dp_mid
	s_setprio 0
	s_branch .Lmy_dp_done

.Lmy_dp_hi:
	s_cmp_gt_i32 s23, 13
	s_cbranch_scc1 .Lmy_dp_top
	s_setprio 2
	s_branch .Lmy_dp_done
